# conversion ring counted vmcnt + no start stagger in the bf16 GEMM phases P1 and P3
# speedup vs baseline: 1.0214x; 1.0125x over previous
.LBB0_87:
	s_cmp_lt_i32 s96, 2
	s_cselect_b64 s[4:5], -1, 0
	v_writelane_b32 v254, s94, 21
	s_and_b64 s[4:5], s[4:5], s[0:1]
	v_writelane_b32 v254, s70, 22
	s_andn2_b64 vcc, exec, s[4:5]
	s_nop 0
	v_writelane_b32 v254, s71, 23
	s_cbranch_vccnz .LBB0_190
	v_mov_b32_e32 v1, v0
	s_mov_b32 s0, 0
	s_cmp_eq_u32 s0, 0
	v_readfirstlane_b32 s13, v1
	s_cbranch_scc1 .LBB0_90

.LBB0_369:
	s_cmp_lt_i32 s96, 4
	s_cselect_b64 s[4:5], -1, 0
	s_and_b64 s[4:5], s[4:5], s[0:1]
	s_andn2_b64 vcc, exec, s[4:5]
	s_cbranch_vccnz .LBB0_395
	s_mov_b32 s0, 0
	v_mov_b32_e32 v1, v0
	s_cmp_eq_u32 s0, 0
	s_cbranch_scc1 .LBB0_372
